# v76 + expert row-tile table (LDS) built in phase M reused by phase N, next layer's phase A and the final phase instead of being rebuilt (one counter round trip + scan removed per phase)
# speedup vs baseline: 1.0012x; 1.0012x over previous
.LBB0_2260:
	s_and_b64 s[2:3], s[8:9], s[4:5]
	s_andn2_b64 vcc, exec, s[2:3]
	s_cbranch_vccnz .LBB0_3232
	v_readlane_b32 s10, v254, 0
	v_readlane_b32 s11, v254, 1
	s_load_dwordx2 s[12:13], s[10:11], 0x120
	s_mov_b32 s0, s43
	v_mov_b32_e32 v128, v235
	v_readlane_b32 s20, v254, 6
	s_cmp_lg_u32 s20, 0
	s_waitcnt vmcnt(0)
	v_and_b32_e32 v34, 63, v128
	s_branch .LBB0_2269

.LBB0_6134:
	v_readlane_b32 s2, v254, 0
	v_readlane_b32 s3, v254, 1
	s_load_dword s0, s[2:3], 0x128
	v_readlane_b32 s4, v254, 50
	s_add_i32 s36, s4, 13
	s_waitcnt lgkmcnt(0)
	s_cmp_le_i32 s0, s36
	s_cbranch_scc0 .LBB0_6987
	s_load_dword s0, s[2:3], 0x12c
	s_waitcnt lgkmcnt(0)
	s_cmp_ge_i32 s36, s0
	s_cbranch_scc1 .LBB0_6987
	v_readlane_b32 s8, v254, 0
	v_readlane_b32 s9, v254, 1
	s_load_dwordx2 s[10:11], s[8:9], 0x120
	s_mov_b32 s6, s43
	v_mov_b32_e32 v216, v235
	v_readlane_b32 s33, v254, 6
	s_cmp_lg_u32 s33, 0
	v_and_b32_e32 v217, 63, v216
	s_branch .LBB0_6144

.LBB0_7064:
	v_readlane_b32 s2, v254, 0
	v_readlane_b32 s3, v254, 1
	s_load_dword s0, s[2:3], 0x128
	s_waitcnt lgkmcnt(0)
	s_cmp_lt_i32 s0, 28
	s_cbranch_scc0 .LBB0_7077
	s_load_dword s0, s[2:3], 0x12c
	s_waitcnt lgkmcnt(0)
	s_cmp_lt_i32 s0, 28
	s_cbranch_scc1 .LBB0_7077
	v_readlane_b32 s0, v254, 0
	v_readlane_b32 s1, v254, 1
	s_load_dwordx2 s[8:9], s[0:1], 0x120
	v_readlane_b32 s6, v254, 6
	s_mov_b64 s[10:11], s[0:1]
	s_cmp_lg_u32 s6, 0
	v_and_b32_e32 v0, 63, v235
	s_branch .LBB0_7074
